# paired select scan without the in-row mask on the fast path (taken only when all 256 keys are inside the row) and v_addc for the second position; on top of v048
# speedup vs baseline: 1.0136x; 1.0101x over previous
.LBB0_1132:
	s_add_i32 s8, s33, 0x180
	s_cmp_gt_i32 s8, s10
	s_cbranch_scc1 .Lsel0_single_0
	s_movk_i32 s96, 0x2c0
	v_and_b32_e32 v7, 0xffff, v63
	v_and_b32_e32 v13, 0xffff, v62
	v_lshrrev_b32_e32 v5, 16, v63
	v_lshrrev_b32_e32 v11, 16, v62
	v_cmp_le_u32_e64 s[18:19], s93, v7
	v_cmp_le_u32_e64 s[8:9], s93, v5
	v_cmp_le_u32_e64 s[46:47], s93, v13
	v_cmp_le_u32_e64 s[58:59], s93, v11
	v_add_u32_e32 v6, 0x80, v2
	v_add_u32_e32 v12, 0x100, v2
	v_mbcnt_lo_u32_b32 v3, s18, 0
	v_mbcnt_hi_u32_b32 v3, s19, v3
	v_mbcnt_lo_u32_b32 v9, s46, 0
	v_mbcnt_hi_u32_b32 v9, s47, v9
	s_bcnt1_i32_b64 s98, s[18:19]
	s_bcnt1_i32_b64 s99, s[8:9]
	v_mbcnt_lo_u32_b32 v3, s8, v3
	v_mbcnt_hi_u32_b32 v3, s9, v3
	s_add_i32 s98, s98, s99
	v_mbcnt_lo_u32_b32 v9, s58, v9
	v_mbcnt_hi_u32_b32 v9, s59, v9
	s_add_i32 s98, s49, s98
	v_add_u32_e32 v3, s49, v3
	v_add_u32_e32 v9, s98, v9
	v_addc_co_u32_e64 v0, s[44:45], 0, v3, s[18:19]
	v_addc_co_u32_e64 v8, s[44:45], 0, v9, s[46:47]
	v_cmp_gt_u32_e64 s[44:45], s96, v3
	v_cmp_gt_u32_e64 s[100:101], s96, v0
	v_cmp_gt_u32_e32 vcc, s96, v9
	s_and_b64 s[18:19], s[18:19], s[44:45]
	s_and_saveexec_b64 s[44:45], s[18:19]
	v_lshl_add_u32 v14, v3, 3, s88
	ds_write_b64 v14, v[6:7]
	s_or_b64 exec, exec, s[44:45]
	s_and_b64 s[8:9], s[8:9], s[100:101]
	v_cmp_gt_u32_e64 s[100:101], s96, v8
	s_and_saveexec_b64 s[44:45], s[8:9]
	v_lshl_add_u32 v14, v0, 3, s88
	v_add_u32_e32 v4, 0x81, v2
	ds_write_b64 v14, v[4:5]
	s_or_b64 exec, exec, s[44:45]
	s_bcnt1_i32_b64 s8, s[46:47]
	s_bcnt1_i32_b64 s9, s[58:59]
	s_and_b64 s[46:47], s[46:47], vcc
	s_and_saveexec_b64 s[44:45], s[46:47]
	v_lshl_add_u32 v14, v9, 3, s88
	ds_write_b64 v14, v[12:13]
	s_or_b64 exec, exec, s[44:45]
	s_and_b64 s[58:59], s[58:59], s[100:101]
	s_and_saveexec_b64 s[44:45], s[58:59]
	v_lshl_add_u32 v14, v8, 3, s88
	v_add_u32_e32 v10, 0x101, v2
	ds_write_b64 v14, v[10:11]
	s_or_b64 exec, exec, s[44:45]
	s_add_i32 s8, s8, s9
	s_add_i32 s49, s98, s8
	s_branch .Lsel0_post_0

.LBB0_1142:
	s_add_i32 s8, s33, 0x280
	s_cmp_gt_i32 s8, s10
	s_cbranch_scc1 .Lsel0_single_2
	s_movk_i32 s96, 0x2c0
	v_and_b32_e32 v7, 0xffff, v61
	v_and_b32_e32 v13, 0xffff, v58
	v_lshrrev_b32_e32 v5, 16, v61
	v_lshrrev_b32_e32 v11, 16, v58
	v_cmp_le_u32_e64 s[18:19], s93, v7
	v_cmp_le_u32_e64 s[8:9], s93, v5
	v_cmp_le_u32_e64 s[46:47], s93, v13
	v_cmp_le_u32_e64 s[58:59], s93, v11
	v_add_u32_e32 v6, 0x180, v2
	v_add_u32_e32 v12, 0x200, v2
	v_mbcnt_lo_u32_b32 v3, s18, 0
	v_mbcnt_hi_u32_b32 v3, s19, v3
	v_mbcnt_lo_u32_b32 v9, s46, 0
	v_mbcnt_hi_u32_b32 v9, s47, v9
	s_bcnt1_i32_b64 s98, s[18:19]
	s_bcnt1_i32_b64 s99, s[8:9]
	v_mbcnt_lo_u32_b32 v3, s8, v3
	v_mbcnt_hi_u32_b32 v3, s9, v3
	s_add_i32 s98, s98, s99
	v_mbcnt_lo_u32_b32 v9, s58, v9
	v_mbcnt_hi_u32_b32 v9, s59, v9
	s_add_i32 s98, s49, s98
	v_add_u32_e32 v3, s49, v3
	v_add_u32_e32 v9, s98, v9
	v_addc_co_u32_e64 v0, s[44:45], 0, v3, s[18:19]
	v_addc_co_u32_e64 v8, s[44:45], 0, v9, s[46:47]
	v_cmp_gt_u32_e64 s[44:45], s96, v3
	v_cmp_gt_u32_e64 s[100:101], s96, v0
	v_cmp_gt_u32_e32 vcc, s96, v9
	s_and_b64 s[18:19], s[18:19], s[44:45]
	s_and_saveexec_b64 s[44:45], s[18:19]
	v_lshl_add_u32 v14, v3, 3, s88
	ds_write_b64 v14, v[6:7]
	s_or_b64 exec, exec, s[44:45]
	s_and_b64 s[8:9], s[8:9], s[100:101]
	v_cmp_gt_u32_e64 s[100:101], s96, v8
	s_and_saveexec_b64 s[44:45], s[8:9]
	v_lshl_add_u32 v14, v0, 3, s88
	v_add_u32_e32 v4, 0x181, v2
	ds_write_b64 v14, v[4:5]
	s_or_b64 exec, exec, s[44:45]
	s_bcnt1_i32_b64 s8, s[46:47]
	s_bcnt1_i32_b64 s9, s[58:59]
	s_and_b64 s[46:47], s[46:47], vcc
	s_and_saveexec_b64 s[44:45], s[46:47]
	v_lshl_add_u32 v14, v9, 3, s88
	ds_write_b64 v14, v[12:13]
	s_or_b64 exec, exec, s[44:45]
	s_and_b64 s[58:59], s[58:59], s[100:101]
	s_and_saveexec_b64 s[44:45], s[58:59]
	v_lshl_add_u32 v14, v8, 3, s88
	v_add_u32_e32 v10, 0x201, v2
	ds_write_b64 v14, v[10:11]
	s_or_b64 exec, exec, s[44:45]
	s_add_i32 s8, s8, s9
	s_add_i32 s49, s98, s8
	s_branch .Lsel0_post_2

.LBB0_1152:
	s_add_i32 s8, s33, 0x380
	s_cmp_gt_i32 s8, s10
	s_cbranch_scc1 .Lsel0_single_4
	s_movk_i32 s96, 0x2c0
	v_and_b32_e32 v7, 0xffff, v59
	v_and_b32_e32 v13, 0xffff, v56
	v_lshrrev_b32_e32 v5, 16, v59
	v_lshrrev_b32_e32 v11, 16, v56
	v_cmp_le_u32_e64 s[18:19], s93, v7
	v_cmp_le_u32_e64 s[8:9], s93, v5
	v_cmp_le_u32_e64 s[46:47], s93, v13
	v_cmp_le_u32_e64 s[58:59], s93, v11
	v_add_u32_e32 v6, 0x280, v2
	v_add_u32_e32 v12, 0x300, v2
	v_mbcnt_lo_u32_b32 v3, s18, 0
	v_mbcnt_hi_u32_b32 v3, s19, v3
	v_mbcnt_lo_u32_b32 v9, s46, 0
	v_mbcnt_hi_u32_b32 v9, s47, v9
	s_bcnt1_i32_b64 s98, s[18:19]
	s_bcnt1_i32_b64 s99, s[8:9]
	v_mbcnt_lo_u32_b32 v3, s8, v3
	v_mbcnt_hi_u32_b32 v3, s9, v3
	s_add_i32 s98, s98, s99
	v_mbcnt_lo_u32_b32 v9, s58, v9
	v_mbcnt_hi_u32_b32 v9, s59, v9
	s_add_i32 s98, s49, s98
	v_add_u32_e32 v3, s49, v3
	v_add_u32_e32 v9, s98, v9
	v_addc_co_u32_e64 v0, s[44:45], 0, v3, s[18:19]
	v_addc_co_u32_e64 v8, s[44:45], 0, v9, s[46:47]
	v_cmp_gt_u32_e64 s[44:45], s96, v3
	v_cmp_gt_u32_e64 s[100:101], s96, v0
	v_cmp_gt_u32_e32 vcc, s96, v9
	s_and_b64 s[18:19], s[18:19], s[44:45]
	s_and_saveexec_b64 s[44:45], s[18:19]
	v_lshl_add_u32 v14, v3, 3, s88
	ds_write_b64 v14, v[6:7]
	s_or_b64 exec, exec, s[44:45]
	s_and_b64 s[8:9], s[8:9], s[100:101]
	v_cmp_gt_u32_e64 s[100:101], s96, v8
	s_and_saveexec_b64 s[44:45], s[8:9]
	v_lshl_add_u32 v14, v0, 3, s88
	v_add_u32_e32 v4, 0x281, v2
	ds_write_b64 v14, v[4:5]
	s_or_b64 exec, exec, s[44:45]
	s_bcnt1_i32_b64 s8, s[46:47]
	s_bcnt1_i32_b64 s9, s[58:59]
	s_and_b64 s[46:47], s[46:47], vcc
	s_and_saveexec_b64 s[44:45], s[46:47]
	v_lshl_add_u32 v14, v9, 3, s88
	ds_write_b64 v14, v[12:13]
	s_or_b64 exec, exec, s[44:45]
	s_and_b64 s[58:59], s[58:59], s[100:101]
	s_and_saveexec_b64 s[44:45], s[58:59]
	v_lshl_add_u32 v14, v8, 3, s88
	v_add_u32_e32 v10, 0x301, v2
	ds_write_b64 v14, v[10:11]
	s_or_b64 exec, exec, s[44:45]
	s_add_i32 s8, s8, s9
	s_add_i32 s49, s98, s8
	s_branch .Lsel0_post_4

.LBB0_1162:
	s_add_i32 s8, s33, 0x480
	s_cmp_gt_i32 s8, s10
	s_cbranch_scc1 .Lsel0_single_6
	s_movk_i32 s96, 0x2c0
	v_and_b32_e32 v7, 0xffff, v57
	v_and_b32_e32 v13, 0xffff, v54
	v_lshrrev_b32_e32 v5, 16, v57
	v_lshrrev_b32_e32 v11, 16, v54
	v_cmp_le_u32_e64 s[18:19], s93, v7
	v_cmp_le_u32_e64 s[8:9], s93, v5
	v_cmp_le_u32_e64 s[46:47], s93, v13
	v_cmp_le_u32_e64 s[58:59], s93, v11
	v_add_u32_e32 v6, 0x380, v2
	v_add_u32_e32 v12, 0x400, v2
	v_mbcnt_lo_u32_b32 v3, s18, 0
	v_mbcnt_hi_u32_b32 v3, s19, v3
	v_mbcnt_lo_u32_b32 v9, s46, 0
	v_mbcnt_hi_u32_b32 v9, s47, v9
	s_bcnt1_i32_b64 s98, s[18:19]
	s_bcnt1_i32_b64 s99, s[8:9]
	v_mbcnt_lo_u32_b32 v3, s8, v3
	v_mbcnt_hi_u32_b32 v3, s9, v3
	s_add_i32 s98, s98, s99
	v_mbcnt_lo_u32_b32 v9, s58, v9
	v_mbcnt_hi_u32_b32 v9, s59, v9
	s_add_i32 s98, s49, s98
	v_add_u32_e32 v3, s49, v3
	v_add_u32_e32 v9, s98, v9
	v_addc_co_u32_e64 v0, s[44:45], 0, v3, s[18:19]
	v_addc_co_u32_e64 v8, s[44:45], 0, v9, s[46:47]
	v_cmp_gt_u32_e64 s[44:45], s96, v3
	v_cmp_gt_u32_e64 s[100:101], s96, v0
	v_cmp_gt_u32_e32 vcc, s96, v9
	s_and_b64 s[18:19], s[18:19], s[44:45]
	s_and_saveexec_b64 s[44:45], s[18:19]
	v_lshl_add_u32 v14, v3, 3, s88
	ds_write_b64 v14, v[6:7]
	s_or_b64 exec, exec, s[44:45]
	s_and_b64 s[8:9], s[8:9], s[100:101]
	v_cmp_gt_u32_e64 s[100:101], s96, v8
	s_and_saveexec_b64 s[44:45], s[8:9]
	v_lshl_add_u32 v14, v0, 3, s88
	v_add_u32_e32 v4, 0x381, v2
	ds_write_b64 v14, v[4:5]
	s_or_b64 exec, exec, s[44:45]
	s_bcnt1_i32_b64 s8, s[46:47]
	s_bcnt1_i32_b64 s9, s[58:59]
	s_and_b64 s[46:47], s[46:47], vcc
	s_and_saveexec_b64 s[44:45], s[46:47]
	v_lshl_add_u32 v14, v9, 3, s88
	ds_write_b64 v14, v[12:13]
	s_or_b64 exec, exec, s[44:45]
	s_and_b64 s[58:59], s[58:59], s[100:101]
	s_and_saveexec_b64 s[44:45], s[58:59]
	v_lshl_add_u32 v14, v8, 3, s88
	v_add_u32_e32 v10, 0x401, v2
	ds_write_b64 v14, v[10:11]
	s_or_b64 exec, exec, s[44:45]
	s_add_i32 s8, s8, s9
	s_add_i32 s49, s98, s8
	s_branch .Lsel0_post_6

.LBB0_1172:
	s_add_i32 s8, s33, 0x580
	s_cmp_gt_i32 s8, s10
	s_cbranch_scc1 .Lsel0_single_8
	s_movk_i32 s96, 0x2c0
	v_and_b32_e32 v7, 0xffff, v55
	v_and_b32_e32 v13, 0xffff, v52
	v_lshrrev_b32_e32 v5, 16, v55
	v_lshrrev_b32_e32 v11, 16, v52
	v_cmp_le_u32_e64 s[18:19], s93, v7
	v_cmp_le_u32_e64 s[8:9], s93, v5
	v_cmp_le_u32_e64 s[46:47], s93, v13
	v_cmp_le_u32_e64 s[58:59], s93, v11
	v_add_u32_e32 v6, 0x480, v2
	v_add_u32_e32 v12, 0x500, v2
	v_mbcnt_lo_u32_b32 v3, s18, 0
	v_mbcnt_hi_u32_b32 v3, s19, v3
	v_mbcnt_lo_u32_b32 v9, s46, 0
	v_mbcnt_hi_u32_b32 v9, s47, v9
	s_bcnt1_i32_b64 s98, s[18:19]
	s_bcnt1_i32_b64 s99, s[8:9]
	v_mbcnt_lo_u32_b32 v3, s8, v3
	v_mbcnt_hi_u32_b32 v3, s9, v3
	s_add_i32 s98, s98, s99
	v_mbcnt_lo_u32_b32 v9, s58, v9
	v_mbcnt_hi_u32_b32 v9, s59, v9
	s_add_i32 s98, s49, s98
	v_add_u32_e32 v3, s49, v3
	v_add_u32_e32 v9, s98, v9
	v_addc_co_u32_e64 v0, s[44:45], 0, v3, s[18:19]
	v_addc_co_u32_e64 v8, s[44:45], 0, v9, s[46:47]
	v_cmp_gt_u32_e64 s[44:45], s96, v3
	v_cmp_gt_u32_e64 s[100:101], s96, v0
	v_cmp_gt_u32_e32 vcc, s96, v9
	s_and_b64 s[18:19], s[18:19], s[44:45]
	s_and_saveexec_b64 s[44:45], s[18:19]
	v_lshl_add_u32 v14, v3, 3, s88
	ds_write_b64 v14, v[6:7]
	s_or_b64 exec, exec, s[44:45]
	s_and_b64 s[8:9], s[8:9], s[100:101]
	v_cmp_gt_u32_e64 s[100:101], s96, v8
	s_and_saveexec_b64 s[44:45], s[8:9]
	v_lshl_add_u32 v14, v0, 3, s88
	v_add_u32_e32 v4, 0x481, v2
	ds_write_b64 v14, v[4:5]
	s_or_b64 exec, exec, s[44:45]
	s_bcnt1_i32_b64 s8, s[46:47]
	s_bcnt1_i32_b64 s9, s[58:59]
	s_and_b64 s[46:47], s[46:47], vcc
	s_and_saveexec_b64 s[44:45], s[46:47]
	v_lshl_add_u32 v14, v9, 3, s88
	ds_write_b64 v14, v[12:13]
	s_or_b64 exec, exec, s[44:45]
	s_and_b64 s[58:59], s[58:59], s[100:101]
	s_and_saveexec_b64 s[44:45], s[58:59]
	v_lshl_add_u32 v14, v8, 3, s88
	v_add_u32_e32 v10, 0x501, v2
	ds_write_b64 v14, v[10:11]
	s_or_b64 exec, exec, s[44:45]
	s_add_i32 s8, s8, s9
	s_add_i32 s49, s98, s8
	s_branch .Lsel0_post_8

.LBB0_1182:
	s_add_i32 s8, s33, 0x680
	s_cmp_gt_i32 s8, s10
	s_cbranch_scc1 .Lsel0_single_10
	s_movk_i32 s96, 0x2c0
	v_and_b32_e32 v7, 0xffff, v53
	v_and_b32_e32 v13, 0xffff, v34
	v_lshrrev_b32_e32 v5, 16, v53
	v_lshrrev_b32_e32 v11, 16, v34
	v_cmp_le_u32_e64 s[18:19], s93, v7
	v_cmp_le_u32_e64 s[8:9], s93, v5
	v_cmp_le_u32_e64 s[46:47], s93, v13
	v_cmp_le_u32_e64 s[58:59], s93, v11
	v_add_u32_e32 v6, 0x580, v2
	v_add_u32_e32 v12, 0x600, v2
	v_mbcnt_lo_u32_b32 v3, s18, 0
	v_mbcnt_hi_u32_b32 v3, s19, v3
	v_mbcnt_lo_u32_b32 v9, s46, 0
	v_mbcnt_hi_u32_b32 v9, s47, v9
	s_bcnt1_i32_b64 s98, s[18:19]
	s_bcnt1_i32_b64 s99, s[8:9]
	v_mbcnt_lo_u32_b32 v3, s8, v3
	v_mbcnt_hi_u32_b32 v3, s9, v3
	s_add_i32 s98, s98, s99
	v_mbcnt_lo_u32_b32 v9, s58, v9
	v_mbcnt_hi_u32_b32 v9, s59, v9
	s_add_i32 s98, s49, s98
	v_add_u32_e32 v3, s49, v3
	v_add_u32_e32 v9, s98, v9
	v_addc_co_u32_e64 v0, s[44:45], 0, v3, s[18:19]
	v_addc_co_u32_e64 v8, s[44:45], 0, v9, s[46:47]
	v_cmp_gt_u32_e64 s[44:45], s96, v3
	v_cmp_gt_u32_e64 s[100:101], s96, v0
	v_cmp_gt_u32_e32 vcc, s96, v9
	s_and_b64 s[18:19], s[18:19], s[44:45]
	s_and_saveexec_b64 s[44:45], s[18:19]
	v_lshl_add_u32 v14, v3, 3, s88
	ds_write_b64 v14, v[6:7]
	s_or_b64 exec, exec, s[44:45]
	s_and_b64 s[8:9], s[8:9], s[100:101]
	v_cmp_gt_u32_e64 s[100:101], s96, v8
	s_and_saveexec_b64 s[44:45], s[8:9]
	v_lshl_add_u32 v14, v0, 3, s88
	v_add_u32_e32 v4, 0x581, v2
	ds_write_b64 v14, v[4:5]
	s_or_b64 exec, exec, s[44:45]
	s_bcnt1_i32_b64 s8, s[46:47]
	s_bcnt1_i32_b64 s9, s[58:59]
	s_and_b64 s[46:47], s[46:47], vcc
	s_and_saveexec_b64 s[44:45], s[46:47]
	v_lshl_add_u32 v14, v9, 3, s88
	ds_write_b64 v14, v[12:13]
	s_or_b64 exec, exec, s[44:45]
	s_and_b64 s[58:59], s[58:59], s[100:101]
	s_and_saveexec_b64 s[44:45], s[58:59]
	v_lshl_add_u32 v14, v8, 3, s88
	v_add_u32_e32 v10, 0x601, v2
	ds_write_b64 v14, v[10:11]
	s_or_b64 exec, exec, s[44:45]
	s_add_i32 s8, s8, s9
	s_add_i32 s49, s98, s8
	s_branch .Lsel0_post_10

.LBB0_1192:
	s_add_i32 s8, s33, 0x780
	s_cmp_gt_i32 s8, s10
	s_cbranch_scc1 .Lsel0_single_12
	s_movk_i32 s96, 0x2c0
	v_and_b32_e32 v7, 0xffff, v35
	v_and_b32_e32 v13, 0xffff, v32
	v_lshrrev_b32_e32 v5, 16, v35
	v_lshrrev_b32_e32 v11, 16, v32
	v_cmp_le_u32_e64 s[18:19], s93, v7
	v_cmp_le_u32_e64 s[8:9], s93, v5
	v_cmp_le_u32_e64 s[46:47], s93, v13
	v_cmp_le_u32_e64 s[58:59], s93, v11
	v_add_u32_e32 v6, 0x680, v2
	v_add_u32_e32 v12, 0x700, v2
	v_mbcnt_lo_u32_b32 v3, s18, 0
	v_mbcnt_hi_u32_b32 v3, s19, v3
	v_mbcnt_lo_u32_b32 v9, s46, 0
	v_mbcnt_hi_u32_b32 v9, s47, v9
	s_bcnt1_i32_b64 s98, s[18:19]
	s_bcnt1_i32_b64 s99, s[8:9]
	v_mbcnt_lo_u32_b32 v3, s8, v3
	v_mbcnt_hi_u32_b32 v3, s9, v3
	s_add_i32 s98, s98, s99
	v_mbcnt_lo_u32_b32 v9, s58, v9
	v_mbcnt_hi_u32_b32 v9, s59, v9
	s_add_i32 s98, s49, s98
	v_add_u32_e32 v3, s49, v3
	v_add_u32_e32 v9, s98, v9
	v_addc_co_u32_e64 v0, s[44:45], 0, v3, s[18:19]
	v_addc_co_u32_e64 v8, s[44:45], 0, v9, s[46:47]
	v_cmp_gt_u32_e64 s[44:45], s96, v3
	v_cmp_gt_u32_e64 s[100:101], s96, v0
	v_cmp_gt_u32_e32 vcc, s96, v9
	s_and_b64 s[18:19], s[18:19], s[44:45]
	s_and_saveexec_b64 s[44:45], s[18:19]
	v_lshl_add_u32 v14, v3, 3, s88
	ds_write_b64 v14, v[6:7]
	s_or_b64 exec, exec, s[44:45]
	s_and_b64 s[8:9], s[8:9], s[100:101]
	v_cmp_gt_u32_e64 s[100:101], s96, v8
	s_and_saveexec_b64 s[44:45], s[8:9]
	v_lshl_add_u32 v14, v0, 3, s88
	v_add_u32_e32 v4, 0x681, v2
	ds_write_b64 v14, v[4:5]
	s_or_b64 exec, exec, s[44:45]
	s_bcnt1_i32_b64 s8, s[46:47]
	s_bcnt1_i32_b64 s9, s[58:59]
	s_and_b64 s[46:47], s[46:47], vcc
	s_and_saveexec_b64 s[44:45], s[46:47]
	v_lshl_add_u32 v14, v9, 3, s88
	ds_write_b64 v14, v[12:13]
	s_or_b64 exec, exec, s[44:45]
	s_and_b64 s[58:59], s[58:59], s[100:101]
	s_and_saveexec_b64 s[44:45], s[58:59]
	v_lshl_add_u32 v14, v8, 3, s88
	v_add_u32_e32 v10, 0x701, v2
	ds_write_b64 v14, v[10:11]
	s_or_b64 exec, exec, s[44:45]
	s_add_i32 s8, s8, s9
	s_add_i32 s49, s98, s8
	s_branch .Lsel0_post_12

.LBB0_1235:
	s_add_i32 s8, s30, 0x180
	s_cmp_gt_i32 s8, s10
	s_cbranch_scc1 .Lsel1_single_0
	s_movk_i32 s96, 0x2c0
	v_and_b32_e32 v7, 0xffff, v17
	v_and_b32_e32 v13, 0xffff, v18
	v_lshrrev_b32_e32 v5, 16, v17
	v_lshrrev_b32_e32 v11, 16, v18
	v_cmp_le_u32_e64 s[18:19], s29, v7
	v_cmp_le_u32_e64 s[8:9], s29, v5
	v_cmp_le_u32_e64 s[46:47], s29, v13
	v_cmp_le_u32_e64 s[58:59], s29, v11
	v_add_u32_e32 v6, 0x80, v2
	v_add_u32_e32 v12, 0x100, v2
	v_mbcnt_lo_u32_b32 v3, s18, 0
	v_mbcnt_hi_u32_b32 v3, s19, v3
	v_mbcnt_lo_u32_b32 v9, s46, 0
	v_mbcnt_hi_u32_b32 v9, s47, v9
	s_bcnt1_i32_b64 s98, s[18:19]
	s_bcnt1_i32_b64 s99, s[8:9]
	v_mbcnt_lo_u32_b32 v3, s8, v3
	v_mbcnt_hi_u32_b32 v3, s9, v3
	s_add_i32 s98, s98, s99
	v_mbcnt_lo_u32_b32 v9, s58, v9
	v_mbcnt_hi_u32_b32 v9, s59, v9
	s_add_i32 s98, s28, s98
	v_add_u32_e32 v3, s28, v3
	v_add_u32_e32 v9, s98, v9
	v_addc_co_u32_e64 v0, s[44:45], 0, v3, s[18:19]
	v_addc_co_u32_e64 v8, s[44:45], 0, v9, s[46:47]
	v_cmp_gt_u32_e64 s[44:45], s96, v3
	v_cmp_gt_u32_e64 s[100:101], s96, v0
	v_cmp_gt_u32_e32 vcc, s96, v9
	s_and_b64 s[18:19], s[18:19], s[44:45]
	s_and_saveexec_b64 s[44:45], s[18:19]
	v_lshl_add_u32 v14, v3, 3, s88
	ds_write_b64 v14, v[6:7]
	s_or_b64 exec, exec, s[44:45]
	s_and_b64 s[8:9], s[8:9], s[100:101]
	v_cmp_gt_u32_e64 s[100:101], s96, v8
	s_and_saveexec_b64 s[44:45], s[8:9]
	v_lshl_add_u32 v14, v0, 3, s88
	v_add_u32_e32 v4, 0x81, v2
	ds_write_b64 v14, v[4:5]
	s_or_b64 exec, exec, s[44:45]
	s_bcnt1_i32_b64 s8, s[46:47]
	s_bcnt1_i32_b64 s9, s[58:59]
	s_and_b64 s[46:47], s[46:47], vcc
	s_and_saveexec_b64 s[44:45], s[46:47]
	v_lshl_add_u32 v14, v9, 3, s88
	ds_write_b64 v14, v[12:13]
	s_or_b64 exec, exec, s[44:45]
	s_and_b64 s[58:59], s[58:59], s[100:101]
	s_and_saveexec_b64 s[44:45], s[58:59]
	v_lshl_add_u32 v14, v8, 3, s88
	v_add_u32_e32 v10, 0x101, v2
	ds_write_b64 v14, v[10:11]
	s_or_b64 exec, exec, s[44:45]
	s_add_i32 s8, s8, s9
	s_add_i32 s28, s98, s8
	s_branch .Lsel1_post_0

.LBB0_1245:
	s_add_i32 s8, s30, 0x280
	s_cmp_gt_i32 s8, s10
	s_cbranch_scc1 .Lsel1_single_2
	s_movk_i32 s96, 0x2c0
	v_and_b32_e32 v7, 0xffff, v19
	v_and_b32_e32 v13, 0xffff, v20
	v_lshrrev_b32_e32 v5, 16, v19
	v_lshrrev_b32_e32 v11, 16, v20
	v_cmp_le_u32_e64 s[18:19], s29, v7
	v_cmp_le_u32_e64 s[8:9], s29, v5
	v_cmp_le_u32_e64 s[46:47], s29, v13
	v_cmp_le_u32_e64 s[58:59], s29, v11
	v_add_u32_e32 v6, 0x180, v2
	v_add_u32_e32 v12, 0x200, v2
	v_mbcnt_lo_u32_b32 v3, s18, 0
	v_mbcnt_hi_u32_b32 v3, s19, v3
	v_mbcnt_lo_u32_b32 v9, s46, 0
	v_mbcnt_hi_u32_b32 v9, s47, v9
	s_bcnt1_i32_b64 s98, s[18:19]
	s_bcnt1_i32_b64 s99, s[8:9]
	v_mbcnt_lo_u32_b32 v3, s8, v3
	v_mbcnt_hi_u32_b32 v3, s9, v3
	s_add_i32 s98, s98, s99
	v_mbcnt_lo_u32_b32 v9, s58, v9
	v_mbcnt_hi_u32_b32 v9, s59, v9
	s_add_i32 s98, s28, s98
	v_add_u32_e32 v3, s28, v3
	v_add_u32_e32 v9, s98, v9
	v_addc_co_u32_e64 v0, s[44:45], 0, v3, s[18:19]
	v_addc_co_u32_e64 v8, s[44:45], 0, v9, s[46:47]
	v_cmp_gt_u32_e64 s[44:45], s96, v3
	v_cmp_gt_u32_e64 s[100:101], s96, v0
	v_cmp_gt_u32_e32 vcc, s96, v9
	s_and_b64 s[18:19], s[18:19], s[44:45]
	s_and_saveexec_b64 s[44:45], s[18:19]
	v_lshl_add_u32 v14, v3, 3, s88
	ds_write_b64 v14, v[6:7]
	s_or_b64 exec, exec, s[44:45]
	s_and_b64 s[8:9], s[8:9], s[100:101]
	v_cmp_gt_u32_e64 s[100:101], s96, v8
	s_and_saveexec_b64 s[44:45], s[8:9]
	v_lshl_add_u32 v14, v0, 3, s88
	v_add_u32_e32 v4, 0x181, v2
	ds_write_b64 v14, v[4:5]
	s_or_b64 exec, exec, s[44:45]
	s_bcnt1_i32_b64 s8, s[46:47]
	s_bcnt1_i32_b64 s9, s[58:59]
	s_and_b64 s[46:47], s[46:47], vcc
	s_and_saveexec_b64 s[44:45], s[46:47]
	v_lshl_add_u32 v14, v9, 3, s88
	ds_write_b64 v14, v[12:13]
	s_or_b64 exec, exec, s[44:45]
	s_and_b64 s[58:59], s[58:59], s[100:101]
	s_and_saveexec_b64 s[44:45], s[58:59]
	v_lshl_add_u32 v14, v8, 3, s88
	v_add_u32_e32 v10, 0x201, v2
	ds_write_b64 v14, v[10:11]
	s_or_b64 exec, exec, s[44:45]
	s_add_i32 s8, s8, s9
	s_add_i32 s28, s98, s8
	s_branch .Lsel1_post_2

.LBB0_1255:
	s_add_i32 s8, s30, 0x380
	s_cmp_gt_i32 s8, s10
	s_cbranch_scc1 .Lsel1_single_4
	s_movk_i32 s96, 0x2c0
	v_and_b32_e32 v7, 0xffff, v21
	v_and_b32_e32 v13, 0xffff, v22
	v_lshrrev_b32_e32 v5, 16, v21
	v_lshrrev_b32_e32 v11, 16, v22
	v_cmp_le_u32_e64 s[18:19], s29, v7
	v_cmp_le_u32_e64 s[8:9], s29, v5
	v_cmp_le_u32_e64 s[46:47], s29, v13
	v_cmp_le_u32_e64 s[58:59], s29, v11
	v_add_u32_e32 v6, 0x280, v2
	v_add_u32_e32 v12, 0x300, v2
	v_mbcnt_lo_u32_b32 v3, s18, 0
	v_mbcnt_hi_u32_b32 v3, s19, v3
	v_mbcnt_lo_u32_b32 v9, s46, 0
	v_mbcnt_hi_u32_b32 v9, s47, v9
	s_bcnt1_i32_b64 s98, s[18:19]
	s_bcnt1_i32_b64 s99, s[8:9]
	v_mbcnt_lo_u32_b32 v3, s8, v3
	v_mbcnt_hi_u32_b32 v3, s9, v3
	s_add_i32 s98, s98, s99
	v_mbcnt_lo_u32_b32 v9, s58, v9
	v_mbcnt_hi_u32_b32 v9, s59, v9
	s_add_i32 s98, s28, s98
	v_add_u32_e32 v3, s28, v3
	v_add_u32_e32 v9, s98, v9
	v_addc_co_u32_e64 v0, s[44:45], 0, v3, s[18:19]
	v_addc_co_u32_e64 v8, s[44:45], 0, v9, s[46:47]
	v_cmp_gt_u32_e64 s[44:45], s96, v3
	v_cmp_gt_u32_e64 s[100:101], s96, v0
	v_cmp_gt_u32_e32 vcc, s96, v9
	s_and_b64 s[18:19], s[18:19], s[44:45]
	s_and_saveexec_b64 s[44:45], s[18:19]
	v_lshl_add_u32 v14, v3, 3, s88
	ds_write_b64 v14, v[6:7]
	s_or_b64 exec, exec, s[44:45]
	s_and_b64 s[8:9], s[8:9], s[100:101]
	v_cmp_gt_u32_e64 s[100:101], s96, v8
	s_and_saveexec_b64 s[44:45], s[8:9]
	v_lshl_add_u32 v14, v0, 3, s88
	v_add_u32_e32 v4, 0x281, v2
	ds_write_b64 v14, v[4:5]
	s_or_b64 exec, exec, s[44:45]
	s_bcnt1_i32_b64 s8, s[46:47]
	s_bcnt1_i32_b64 s9, s[58:59]
	s_and_b64 s[46:47], s[46:47], vcc
	s_and_saveexec_b64 s[44:45], s[46:47]
	v_lshl_add_u32 v14, v9, 3, s88
	ds_write_b64 v14, v[12:13]
	s_or_b64 exec, exec, s[44:45]
	s_and_b64 s[58:59], s[58:59], s[100:101]
	s_and_saveexec_b64 s[44:45], s[58:59]
	v_lshl_add_u32 v14, v8, 3, s88
	v_add_u32_e32 v10, 0x301, v2
	ds_write_b64 v14, v[10:11]
	s_or_b64 exec, exec, s[44:45]
	s_add_i32 s8, s8, s9
	s_add_i32 s28, s98, s8
	s_branch .Lsel1_post_4

.LBB0_1265:
	s_add_i32 s8, s30, 0x480
	s_cmp_gt_i32 s8, s10
	s_cbranch_scc1 .Lsel1_single_6
	s_movk_i32 s96, 0x2c0
	v_and_b32_e32 v7, 0xffff, v23
	v_and_b32_e32 v13, 0xffff, v24
	v_lshrrev_b32_e32 v5, 16, v23
	v_lshrrev_b32_e32 v11, 16, v24
	v_cmp_le_u32_e64 s[18:19], s29, v7
	v_cmp_le_u32_e64 s[8:9], s29, v5
	v_cmp_le_u32_e64 s[46:47], s29, v13
	v_cmp_le_u32_e64 s[58:59], s29, v11
	v_add_u32_e32 v6, 0x380, v2
	v_add_u32_e32 v12, 0x400, v2
	v_mbcnt_lo_u32_b32 v3, s18, 0
	v_mbcnt_hi_u32_b32 v3, s19, v3
	v_mbcnt_lo_u32_b32 v9, s46, 0
	v_mbcnt_hi_u32_b32 v9, s47, v9
	s_bcnt1_i32_b64 s98, s[18:19]
	s_bcnt1_i32_b64 s99, s[8:9]
	v_mbcnt_lo_u32_b32 v3, s8, v3
	v_mbcnt_hi_u32_b32 v3, s9, v3
	s_add_i32 s98, s98, s99
	v_mbcnt_lo_u32_b32 v9, s58, v9
	v_mbcnt_hi_u32_b32 v9, s59, v9
	s_add_i32 s98, s28, s98
	v_add_u32_e32 v3, s28, v3
	v_add_u32_e32 v9, s98, v9
	v_addc_co_u32_e64 v0, s[44:45], 0, v3, s[18:19]
	v_addc_co_u32_e64 v8, s[44:45], 0, v9, s[46:47]
	v_cmp_gt_u32_e64 s[44:45], s96, v3
	v_cmp_gt_u32_e64 s[100:101], s96, v0
	v_cmp_gt_u32_e32 vcc, s96, v9
	s_and_b64 s[18:19], s[18:19], s[44:45]
	s_and_saveexec_b64 s[44:45], s[18:19]
	v_lshl_add_u32 v14, v3, 3, s88
	ds_write_b64 v14, v[6:7]
	s_or_b64 exec, exec, s[44:45]
	s_and_b64 s[8:9], s[8:9], s[100:101]
	v_cmp_gt_u32_e64 s[100:101], s96, v8
	s_and_saveexec_b64 s[44:45], s[8:9]
	v_lshl_add_u32 v14, v0, 3, s88
	v_add_u32_e32 v4, 0x381, v2
	ds_write_b64 v14, v[4:5]
	s_or_b64 exec, exec, s[44:45]
	s_bcnt1_i32_b64 s8, s[46:47]
	s_bcnt1_i32_b64 s9, s[58:59]
	s_and_b64 s[46:47], s[46:47], vcc
	s_and_saveexec_b64 s[44:45], s[46:47]
	v_lshl_add_u32 v14, v9, 3, s88
	ds_write_b64 v14, v[12:13]
	s_or_b64 exec, exec, s[44:45]
	s_and_b64 s[58:59], s[58:59], s[100:101]
	s_and_saveexec_b64 s[44:45], s[58:59]
	v_lshl_add_u32 v14, v8, 3, s88
	v_add_u32_e32 v10, 0x401, v2
	ds_write_b64 v14, v[10:11]
	s_or_b64 exec, exec, s[44:45]
	s_add_i32 s8, s8, s9
	s_add_i32 s28, s98, s8
	s_branch .Lsel1_post_6

.LBB0_1275:
	s_add_i32 s8, s30, 0x580
	s_cmp_gt_i32 s8, s10
	s_cbranch_scc1 .Lsel1_single_8
	s_movk_i32 s96, 0x2c0
	v_and_b32_e32 v7, 0xffff, v25
	v_and_b32_e32 v13, 0xffff, v26
	v_lshrrev_b32_e32 v5, 16, v25
	v_lshrrev_b32_e32 v11, 16, v26
	v_cmp_le_u32_e64 s[18:19], s29, v7
	v_cmp_le_u32_e64 s[8:9], s29, v5
	v_cmp_le_u32_e64 s[46:47], s29, v13
	v_cmp_le_u32_e64 s[58:59], s29, v11
	v_add_u32_e32 v6, 0x480, v2
	v_add_u32_e32 v12, 0x500, v2
	v_mbcnt_lo_u32_b32 v3, s18, 0
	v_mbcnt_hi_u32_b32 v3, s19, v3
	v_mbcnt_lo_u32_b32 v9, s46, 0
	v_mbcnt_hi_u32_b32 v9, s47, v9
	s_bcnt1_i32_b64 s98, s[18:19]
	s_bcnt1_i32_b64 s99, s[8:9]
	v_mbcnt_lo_u32_b32 v3, s8, v3
	v_mbcnt_hi_u32_b32 v3, s9, v3
	s_add_i32 s98, s98, s99
	v_mbcnt_lo_u32_b32 v9, s58, v9
	v_mbcnt_hi_u32_b32 v9, s59, v9
	s_add_i32 s98, s28, s98
	v_add_u32_e32 v3, s28, v3
	v_add_u32_e32 v9, s98, v9
	v_addc_co_u32_e64 v0, s[44:45], 0, v3, s[18:19]
	v_addc_co_u32_e64 v8, s[44:45], 0, v9, s[46:47]
	v_cmp_gt_u32_e64 s[44:45], s96, v3
	v_cmp_gt_u32_e64 s[100:101], s96, v0
	v_cmp_gt_u32_e32 vcc, s96, v9
	s_and_b64 s[18:19], s[18:19], s[44:45]
	s_and_saveexec_b64 s[44:45], s[18:19]
	v_lshl_add_u32 v14, v3, 3, s88
	ds_write_b64 v14, v[6:7]
	s_or_b64 exec, exec, s[44:45]
	s_and_b64 s[8:9], s[8:9], s[100:101]
	v_cmp_gt_u32_e64 s[100:101], s96, v8
	s_and_saveexec_b64 s[44:45], s[8:9]
	v_lshl_add_u32 v14, v0, 3, s88
	v_add_u32_e32 v4, 0x481, v2
	ds_write_b64 v14, v[4:5]
	s_or_b64 exec, exec, s[44:45]
	s_bcnt1_i32_b64 s8, s[46:47]
	s_bcnt1_i32_b64 s9, s[58:59]
	s_and_b64 s[46:47], s[46:47], vcc
	s_and_saveexec_b64 s[44:45], s[46:47]
	v_lshl_add_u32 v14, v9, 3, s88
	ds_write_b64 v14, v[12:13]
	s_or_b64 exec, exec, s[44:45]
	s_and_b64 s[58:59], s[58:59], s[100:101]
	s_and_saveexec_b64 s[44:45], s[58:59]
	v_lshl_add_u32 v14, v8, 3, s88
	v_add_u32_e32 v10, 0x501, v2
	ds_write_b64 v14, v[10:11]
	s_or_b64 exec, exec, s[44:45]
	s_add_i32 s8, s8, s9
	s_add_i32 s28, s98, s8
	s_branch .Lsel1_post_8

.LBB0_1285:
	s_add_i32 s8, s30, 0x680
	s_cmp_gt_i32 s8, s10
	s_cbranch_scc1 .Lsel1_single_10
	s_movk_i32 s96, 0x2c0
	v_and_b32_e32 v7, 0xffff, v27
	v_and_b32_e32 v13, 0xffff, v28
	v_lshrrev_b32_e32 v5, 16, v27
	v_lshrrev_b32_e32 v11, 16, v28
	v_cmp_le_u32_e64 s[18:19], s29, v7
	v_cmp_le_u32_e64 s[8:9], s29, v5
	v_cmp_le_u32_e64 s[46:47], s29, v13
	v_cmp_le_u32_e64 s[58:59], s29, v11
	v_add_u32_e32 v6, 0x580, v2
	v_add_u32_e32 v12, 0x600, v2
	v_mbcnt_lo_u32_b32 v3, s18, 0
	v_mbcnt_hi_u32_b32 v3, s19, v3
	v_mbcnt_lo_u32_b32 v9, s46, 0
	v_mbcnt_hi_u32_b32 v9, s47, v9
	s_bcnt1_i32_b64 s98, s[18:19]
	s_bcnt1_i32_b64 s99, s[8:9]
	v_mbcnt_lo_u32_b32 v3, s8, v3
	v_mbcnt_hi_u32_b32 v3, s9, v3
	s_add_i32 s98, s98, s99
	v_mbcnt_lo_u32_b32 v9, s58, v9
	v_mbcnt_hi_u32_b32 v9, s59, v9
	s_add_i32 s98, s28, s98
	v_add_u32_e32 v3, s28, v3
	v_add_u32_e32 v9, s98, v9
	v_addc_co_u32_e64 v0, s[44:45], 0, v3, s[18:19]
	v_addc_co_u32_e64 v8, s[44:45], 0, v9, s[46:47]
	v_cmp_gt_u32_e64 s[44:45], s96, v3
	v_cmp_gt_u32_e64 s[100:101], s96, v0
	v_cmp_gt_u32_e32 vcc, s96, v9
	s_and_b64 s[18:19], s[18:19], s[44:45]
	s_and_saveexec_b64 s[44:45], s[18:19]
	v_lshl_add_u32 v14, v3, 3, s88
	ds_write_b64 v14, v[6:7]
	s_or_b64 exec, exec, s[44:45]
	s_and_b64 s[8:9], s[8:9], s[100:101]
	v_cmp_gt_u32_e64 s[100:101], s96, v8
	s_and_saveexec_b64 s[44:45], s[8:9]
	v_lshl_add_u32 v14, v0, 3, s88
	v_add_u32_e32 v4, 0x581, v2
	ds_write_b64 v14, v[4:5]
	s_or_b64 exec, exec, s[44:45]
	s_bcnt1_i32_b64 s8, s[46:47]
	s_bcnt1_i32_b64 s9, s[58:59]
	s_and_b64 s[46:47], s[46:47], vcc
	s_and_saveexec_b64 s[44:45], s[46:47]
	v_lshl_add_u32 v14, v9, 3, s88
	ds_write_b64 v14, v[12:13]
	s_or_b64 exec, exec, s[44:45]
	s_and_b64 s[58:59], s[58:59], s[100:101]
	s_and_saveexec_b64 s[44:45], s[58:59]
	v_lshl_add_u32 v14, v8, 3, s88
	v_add_u32_e32 v10, 0x601, v2
	ds_write_b64 v14, v[10:11]
	s_or_b64 exec, exec, s[44:45]
	s_add_i32 s8, s8, s9
	s_add_i32 s28, s98, s8
	s_branch .Lsel1_post_10

.LBB0_1295:
	s_add_i32 s8, s30, 0x780
	s_cmp_gt_i32 s8, s10
	s_cbranch_scc1 .Lsel1_single_12
	s_movk_i32 s96, 0x2c0
	v_and_b32_e32 v7, 0xffff, v29
	v_and_b32_e32 v13, 0xffff, v30
	v_lshrrev_b32_e32 v5, 16, v29
	v_lshrrev_b32_e32 v11, 16, v30
	v_cmp_le_u32_e64 s[18:19], s29, v7
	v_cmp_le_u32_e64 s[8:9], s29, v5
	v_cmp_le_u32_e64 s[46:47], s29, v13
	v_cmp_le_u32_e64 s[58:59], s29, v11
	v_add_u32_e32 v6, 0x680, v2
	v_add_u32_e32 v12, 0x700, v2
	v_mbcnt_lo_u32_b32 v3, s18, 0
	v_mbcnt_hi_u32_b32 v3, s19, v3
	v_mbcnt_lo_u32_b32 v9, s46, 0
	v_mbcnt_hi_u32_b32 v9, s47, v9
	s_bcnt1_i32_b64 s98, s[18:19]
	s_bcnt1_i32_b64 s99, s[8:9]
	v_mbcnt_lo_u32_b32 v3, s8, v3
	v_mbcnt_hi_u32_b32 v3, s9, v3
	s_add_i32 s98, s98, s99
	v_mbcnt_lo_u32_b32 v9, s58, v9
	v_mbcnt_hi_u32_b32 v9, s59, v9
	s_add_i32 s98, s28, s98
	v_add_u32_e32 v3, s28, v3
	v_add_u32_e32 v9, s98, v9
	v_addc_co_u32_e64 v0, s[44:45], 0, v3, s[18:19]
	v_addc_co_u32_e64 v8, s[44:45], 0, v9, s[46:47]
	v_cmp_gt_u32_e64 s[44:45], s96, v3
	v_cmp_gt_u32_e64 s[100:101], s96, v0
	v_cmp_gt_u32_e32 vcc, s96, v9
	s_and_b64 s[18:19], s[18:19], s[44:45]
	s_and_saveexec_b64 s[44:45], s[18:19]
	v_lshl_add_u32 v14, v3, 3, s88
	ds_write_b64 v14, v[6:7]
	s_or_b64 exec, exec, s[44:45]
	s_and_b64 s[8:9], s[8:9], s[100:101]
	v_cmp_gt_u32_e64 s[100:101], s96, v8
	s_and_saveexec_b64 s[44:45], s[8:9]
	v_lshl_add_u32 v14, v0, 3, s88
	v_add_u32_e32 v4, 0x681, v2
	ds_write_b64 v14, v[4:5]
	s_or_b64 exec, exec, s[44:45]
	s_bcnt1_i32_b64 s8, s[46:47]
	s_bcnt1_i32_b64 s9, s[58:59]
	s_and_b64 s[46:47], s[46:47], vcc
	s_and_saveexec_b64 s[44:45], s[46:47]
	v_lshl_add_u32 v14, v9, 3, s88
	ds_write_b64 v14, v[12:13]
	s_or_b64 exec, exec, s[44:45]
	s_and_b64 s[58:59], s[58:59], s[100:101]
	s_and_saveexec_b64 s[44:45], s[58:59]
	v_lshl_add_u32 v14, v8, 3, s88
	v_add_u32_e32 v10, 0x701, v2
	ds_write_b64 v14, v[10:11]
	s_or_b64 exec, exec, s[44:45]
	s_add_i32 s8, s8, s9
	s_add_i32 s28, s98, s8
	s_branch .Lsel1_post_12
